# MLA unit setup: tile-0 K/V loads issued together with the Q loads (one exposed global-load latency less per unit half)
# baseline (speedup 1.0000x reference)
; #define LAS __attribute__((address_space(3)))
; __device__ __forceinline__ unsigned f2bf(float f) { unsigned u = __builtin_bit_cast(unsigned, f); return (u + 0x7fffu + ((u >> 16) & 1u)) >> 16; }
; __device__ __forceinline__ float bf2f(bf16 b) { return __uint_as_float(((unsigned)b) << 16); }
; __device__ __forceinline__ void mla_attn_phase(LAS unsigned char* lds, const bf16* Q, const bf16* KV, const bf16* Z, bf16* Oabc, const float* ropec, const float* ropes, int vcu, int G, int tid) {
;     ...
;             { bf16x8 qrope[4]; unsigned qoff_ = qoff, roff_ = roff; asm volatile("" : "+v"(qoff_), "+v"(roff_));
;               const char* Qu = (const char*)(Q + (tok0 + qb * 256) * 1536 + h * 192);
;               const char* cu = (const char*)(ropec + (size_t)(qb * 256) * 32); const char* su = (const char*)(ropes + (size_t)(qb * 256) * 32);
; #pragma unroll
;               for (int d0 = 0; d0 < 8; ++d0) qr[d0] = *(const bf16x8*)(Qu + qoff_ + d0 * 32);
; #pragma unroll
;               for (int d0 = 0; d0 < 4; ++d0) qrope[d0] = *(const bf16x8*)(Qu + qoff_ + (8 + d0) * 32);
; #pragma unroll
;               for (int pr = 0; pr < 2; ++pr) {
;                   const f32x4 c0 = *(const f32x4*)(cu + roff_ + pr * 64), c1 = *(const f32x4*)(cu + roff_ + pr * 64 + 16), s0 = *(const f32x4*)(su + roff_ + pr * 64), s1 = *(const f32x4*)(su + roff_ + pr * 64 + 16);
;                   const float cc[8] = {c0.x, c0.y, c0.z, c0.w, c1.x, c1.y, c1.z, c1.w}, ss[8] = {s0.x, s0.y, s0.z, s0.w, s1.x, s1.y, s1.z, s1.w};
;                   bf16x8 xa = qrope[pr], xb = qrope[2 + pr];
; #pragma unroll
;                   for (int e = 0; e < 8; ++e) { const float x1 = bf2f((bf16)xa[e]), x2 = bf2f((bf16)xb[e]);
;                       xa[e] = (short)f2bf(x1 * cc[e] - x2 * ss[e]); xb[e] = (short)f2bf(x1 * ss[e] + x2 * cc[e]); }
;                   *(LAS bf16x8*)(qrl + (pr * 64 + lane) * 16) = xa; *(LAS bf16x8*)(qrl + ((2 + pr) * 64 + lane) * 16) = xb; } }
;             v4u vs0, vs1, ks0, ks1, krr;
;             const char* KVu = (const char*)(KV + tok0 * 2048 + h * 256); const char* Zu = (const char*)(Z + tok0 * NABC);
.LBB0_1124:
	s_xor_b64 s[12:13], s[6:7], -1
	s_and_b64 s[6:7], s[6:7], exec
	s_cselect_b32 s17, s29, s30
	s_lshl_b32 s16, s17, 8
	s_or_b32 s38, s10, s16
	s_mul_hi_u32 s7, s38, 0xc00
	s_mul_i32 s14, s11, 0xc00
	s_mul_i32 s6, s38, 0xc00
	s_add_i32 s7, s7, s14
	s_add_u32 s14, s31, s6
	s_addc_u32 s15, s34, s7
	s_lshl_b32 s44, s17, 15
	v_mov_b32_e32 v6, v207
	v_mov_b32_e32 v0, v208
	s_add_u32 s6, s20, s44
	s_addc_u32 s7, s21, 0
	global_load_dwordx4 v[112:115], v6, s[14:15]
	global_load_dwordx4 v[116:119], v6, s[14:15] offset:32
	global_load_dwordx4 v[120:123], v6, s[14:15] offset:64
	global_load_dwordx4 v[124:127], v6, s[14:15] offset:96
	global_load_dwordx4 v[128:131], v6, s[14:15] offset:128
	global_load_dwordx4 v[132:135], v6, s[14:15] offset:160
	global_load_dwordx4 v[136:139], v6, s[14:15] offset:192
	global_load_dwordx4 v[140:143], v6, s[14:15] offset:224
	global_load_dwordx4 v[10:13], v6, s[14:15] offset:256
	global_load_dwordx4 v[2:5], v6, s[14:15] offset:288
	global_load_dwordx4 v[14:17], v6, s[14:15] offset:320
	s_nop 0
	global_load_dwordx4 v[6:9], v6, s[14:15] offset:352
	s_add_u32 s14, s22, s44
	s_addc_u32 s15, s23, 0
	global_load_dwordx4 v[18:21], v0, s[6:7] offset:16
	global_load_dwordx4 v[22:25], v0, s[6:7]
	global_load_dwordx4 v[26:29], v0, s[14:15] offset:16
	global_load_dwordx4 v[30:33], v0, s[14:15]
	v_add_u32_e32 v214, s25, v209
	s_mov_b32 s39, s11
	v_add_u32_e32 v215, s16, v205
	v_mov_b32_e32 v217, 0
	v_mov_b32_e32 v216, 0xf149f2ca
	s_mov_b32 s50, 1
	v_mov_b64_e32 v[194:195], v[192:193]
	v_mov_b64_e32 v[196:197], v[190:191]
	global_load_dwordx4 v[144:147], v[172:173], off
	global_load_dwordx4 v[148:151], v[172:173], off offset:256
	global_load_dwordx4 v[152:155], v[174:175], off
	global_load_dwordx4 v[156:159], v[174:175], off offset:256
	global_load_dwordx4 v[160:163], v[176:177], off
	s_waitcnt vmcnt(5)
	v_and_b32_e32 v35, 0xffff0000, v10
	v_lshlrev_b32_e32 v34, 16, v10
	v_and_b32_e32 v37, 0xffff0000, v14
	v_lshlrev_b32_e32 v36, 16, v14
	v_lshlrev_b32_e32 v10, 16, v15
	v_pk_mul_f32 v[38:39], v[30:31], v[34:35]
	v_pk_mul_f32 v[30:31], v[30:31], v[36:37]
	v_pk_fma_f32 v[38:39], v[22:23], v[36:37], v[38:39]
	v_pk_fma_f32 v[22:23], v[22:23], v[34:35], v[30:31] neg_lo:[0,0,1] neg_hi:[0,0,1]
	v_and_b32_e32 v31, 0xffff0000, v11
	v_lshlrev_b32_e32 v30, 16, v11
	v_and_b32_e32 v11, 0xffff0000, v15
	v_pk_mul_f32 v[14:15], v[32:33], v[30:31]
	s_nop 0
	v_pk_fma_f32 v[14:15], v[24:25], v[10:11], v[14:15]
	v_pk_mul_f32 v[10:11], v[32:33], v[10:11]
	s_nop 0
	v_pk_fma_f32 v[10:11], v[24:25], v[30:31], v[10:11] neg_lo:[0,0,1] neg_hi:[0,0,1]
	v_and_b32_e32 v25, 0xffff0000, v12
	v_lshlrev_b32_e32 v24, 16, v12
	v_and_b32_e32 v31, 0xffff0000, v16
	v_lshlrev_b32_e32 v30, 16, v16
	v_pk_mul_f32 v[32:33], v[26:27], v[24:25]
	v_pk_mul_f32 v[26:27], v[26:27], v[30:31]
	v_pk_fma_f32 v[32:33], v[18:19], v[30:31], v[32:33]
	v_pk_fma_f32 v[18:19], v[18:19], v[24:25], v[26:27] neg_lo:[0,0,1] neg_hi:[0,0,1]
	v_and_b32_e32 v25, 0xffff0000, v13
	v_lshlrev_b32_e32 v24, 16, v13
	v_and_b32_e32 v13, 0xffff0000, v17
	v_lshlrev_b32_e32 v12, 16, v17
	v_pk_mul_f32 v[16:17], v[28:29], v[24:25]
	v_bfe_u32 v26, v11, 16, 1
	v_pk_fma_f32 v[16:17], v[20:21], v[12:13], v[16:17]
	v_pk_mul_f32 v[12:13], v[28:29], v[12:13]
	v_bfe_u32 v27, v10, 16, 1
	v_pk_fma_f32 v[12:13], v[20:21], v[24:25], v[12:13] neg_lo:[0,0,1] neg_hi:[0,0,1]
	v_bfe_u32 v24, v19, 16, 1
	v_bfe_u32 v20, v13, 16, 1
	v_bfe_u32 v21, v12, 16, 1
	v_bfe_u32 v25, v18, 16, 1
	v_bfe_u32 v28, v23, 16, 1
	v_bfe_u32 v29, v22, 16, 1
	v_add3_u32 v22, v22, v29, s40
	v_add3_u32 v23, v23, v28, s40
	v_add3_u32 v10, v10, v27, s40
	v_add3_u32 v11, v11, v26, s40
	v_add3_u32 v18, v18, v25, s40
	v_add3_u32 v19, v19, v24, s40
	v_add3_u32 v12, v12, v21, s40
	v_add3_u32 v13, v13, v20, s40
	v_perm_b32 v13, v13, v12, s48
	v_perm_b32 v12, v19, v18, s48
	v_perm_b32 v11, v11, v10, s48
	v_perm_b32 v10, v23, v22, s48
	v_bfe_u32 v18, v17, 16, 1
	v_bfe_u32 v19, v16, 16, 1
	v_bfe_u32 v20, v33, 16, 1
	v_bfe_u32 v21, v32, 16, 1
	v_bfe_u32 v22, v15, 16, 1
	v_bfe_u32 v23, v14, 16, 1
	v_bfe_u32 v24, v39, 16, 1
	v_bfe_u32 v25, v38, 16, 1
	v_add3_u32 v25, v38, v25, s40
	v_add3_u32 v24, v39, v24, s40
	v_add3_u32 v14, v14, v23, s40
	v_add3_u32 v15, v15, v22, s40
	v_add3_u32 v21, v32, v21, s40
	v_add3_u32 v20, v33, v20, s40
	v_add3_u32 v16, v16, v19, s40
	v_add3_u32 v17, v17, v18, s40
	v_perm_b32 v17, v17, v16, s48
	v_perm_b32 v16, v20, v21, s48
	v_perm_b32 v15, v15, v14, s48
	v_perm_b32 v14, v24, v25, s48
	ds_write_b128 v214, v[10:13]
	ds_write_b128 v214, v[14:17] offset:2048
	global_load_dwordx4 v[10:13], v0, s[6:7] offset:80
	global_load_dwordx4 v[14:17], v0, s[6:7] offset:64
	global_load_dwordx4 v[18:21], v0, s[14:15] offset:80
	global_load_dwordx4 v[22:25], v0, s[14:15] offset:64
	v_and_b32_e32 v27, 0xffff0000, v2
	v_lshlrev_b32_e32 v26, 16, v2
	v_and_b32_e32 v29, 0xffff0000, v6
	v_lshlrev_b32_e32 v28, 16, v6
	v_lshlrev_b32_e32 v2, 16, v7
	s_lshl_b32 s6, s17, 2
	s_add_i32 s44, s6, 4
	s_sub_i32 s45, 0, s6
	s_waitcnt vmcnt(0)
; #define LAS __attribute__((address_space(3)))
; __device__ __forceinline__ unsigned f2bf(float f) { unsigned u = __builtin_bit_cast(unsigned, f); return (u + 0x7fffu + ((u >> 16) & 1u)) >> 16; }
; __device__ __forceinline__ float bf2f(bf16 b) { return __uint_as_float(((unsigned)b) << 16); }
; #define MLA_SLOAD(k0) do { const char* kvp = KVu + (size_t)(k0) * 4096; const char* zp = Zu + (size_t)(k0) * (NABC * 2); \
;             ks0 = *(const v4u*)(kvp + kvoff); vs0 = *(const v4u*)(kvp + kvoff + 256); ks1 = *(const v4u*)(kvp + 32 * 4096 + kvoff); vs1 = *(const v4u*)(kvp + 32 * 4096 + kvoff + 256); \
;             krr = *(const v4u*)(zp + zoff); } while (0)
; #define MLA_SWRITE(bb) do { *(LAS v4u*)(V_lds + (bb) * SHM_V + vst0) = vs0; *(LAS v4u*)(V_lds + (bb) * SHM_V + vst0 + 8192) = vs1; \
;             *(LAS v4u*)(K_lds + (bb) * SHM_K + kst0) = ks0; *(LAS v4u*)(K_lds + (bb) * SHM_K + kst0 + 32 * 384) = ks1; \
;             *(LAS v4u*)(K_lds + (bb) * SHM_K + kst2) = krr; } while (0)
; __device__ __forceinline__ void mla_attn_phase(LAS unsigned char* lds, const bf16* Q, const bf16* KV, const bf16* Z, bf16* Oabc, const float* ropec, const float* ropes, int vcu, int G, int tid) {
;     ...
;                   for (int e = 0; e < 8; ++e) { const float x1 = bf2f((bf16)xa[e]), x2 = bf2f((bf16)xb[e]);
;                       xa[e] = (short)f2bf(x1 * cc[e] - x2 * ss[e]); xb[e] = (short)f2bf(x1 * ss[e] + x2 * cc[e]); }
;                   *(LAS bf16x8*)(qrl + (pr * 64 + lane) * 16) = xa; *(LAS bf16x8*)(qrl + ((2 + pr) * 64 + lane) * 16) = xb; } }
;             v4u vs0, vs1, ks0, ks1, krr;
;             const char* KVu = (const char*)(KV + tok0 * 2048 + h * 256); const char* Zu = (const char*)(Z + tok0 * NABC);
;     ...
;             const int nt = 4 * qb + 4;
;             float m_reg = -1e30f, l_reg = 0.f; f32x16 o[4];
; #pragma unroll
;             for (int d = 0; d < 4; ++d)
; #pragma unroll
;                 for (int r = 0; r < 16; ++r) o[d][r] = 0.f;
;             MLA_SLOAD(0); MLA_SWRITE(0); __syncthreads();
	v_pk_mul_f32 v[30:31], v[22:23], v[26:27]
	v_pk_mul_f32 v[22:23], v[22:23], v[28:29]
	v_pk_fma_f32 v[30:31], v[14:15], v[28:29], v[30:31]
	v_pk_fma_f32 v[14:15], v[14:15], v[26:27], v[22:23] neg_lo:[0,0,1] neg_hi:[0,0,1]
	v_and_b32_e32 v23, 0xffff0000, v3
	v_lshlrev_b32_e32 v22, 16, v3
	v_and_b32_e32 v3, 0xffff0000, v7
	v_pk_mul_f32 v[6:7], v[24:25], v[22:23]
	s_nop 0
	v_pk_fma_f32 v[6:7], v[16:17], v[2:3], v[6:7]
	v_pk_mul_f32 v[2:3], v[24:25], v[2:3]
	s_nop 0
	v_pk_fma_f32 v[2:3], v[16:17], v[22:23], v[2:3] neg_lo:[0,0,1] neg_hi:[0,0,1]
	v_and_b32_e32 v17, 0xffff0000, v4
	v_lshlrev_b32_e32 v16, 16, v4
	v_and_b32_e32 v23, 0xffff0000, v8
	v_lshlrev_b32_e32 v22, 16, v8
	v_pk_mul_f32 v[24:25], v[18:19], v[16:17]
	v_pk_mul_f32 v[18:19], v[18:19], v[22:23]
	v_pk_fma_f32 v[24:25], v[10:11], v[22:23], v[24:25]
	v_pk_fma_f32 v[10:11], v[10:11], v[16:17], v[18:19] neg_lo:[0,0,1] neg_hi:[0,0,1]
	v_and_b32_e32 v17, 0xffff0000, v5
	v_lshlrev_b32_e32 v16, 16, v5
	v_and_b32_e32 v5, 0xffff0000, v9
	v_lshlrev_b32_e32 v4, 16, v9
	v_pk_mul_f32 v[8:9], v[20:21], v[16:17]
	v_bfe_u32 v0, v11, 16, 1
	v_pk_fma_f32 v[8:9], v[12:13], v[4:5], v[8:9]
	v_pk_mul_f32 v[4:5], v[20:21], v[4:5]
	v_bfe_u32 v20, v2, 16, 1
	v_pk_fma_f32 v[4:5], v[12:13], v[16:17], v[4:5] neg_lo:[0,0,1] neg_hi:[0,0,1]
	v_bfe_u32 v12, v10, 16, 1
	v_bfe_u32 v13, v15, 16, 1
	v_bfe_u32 v16, v14, 16, 1
	v_bfe_u32 v18, v4, 16, 1
	v_bfe_u32 v17, v5, 16, 1
	v_bfe_u32 v19, v3, 16, 1
	v_add3_u32 v20, v2, v20, s40
	v_add3_u32 v18, v4, v18, s40
	v_add3_u32 v2, v14, v16, s40
	v_add3_u32 v13, v15, v13, s40
	v_add3_u32 v4, v10, v12, s40
	v_add3_u32 v0, v11, v0, s40
	v_add3_u32 v3, v3, v19, s40
	v_add3_u32 v5, v5, v17, s40
	v_perm_b32 v4, v0, v4, s48
	v_perm_b32 v2, v13, v2, s48
	v_bfe_u32 v0, v25, 16, 1
	v_bfe_u32 v10, v24, 16, 1
	v_bfe_u32 v11, v31, 16, 1
	v_bfe_u32 v12, v30, 16, 1
	v_bfe_u32 v13, v9, 16, 1
	v_bfe_u32 v14, v8, 16, 1
	v_bfe_u32 v15, v7, 16, 1
	v_bfe_u32 v16, v6, 16, 1
	v_perm_b32 v5, v5, v18, s48
	v_perm_b32 v3, v3, v20, s48
	v_add3_u32 v16, v6, v16, s40
	v_add3_u32 v7, v7, v15, s40
	v_add3_u32 v14, v8, v14, s40
	v_add3_u32 v9, v9, v13, s40
	v_add3_u32 v6, v30, v12, s40
	v_add3_u32 v11, v31, v11, s40
	v_add3_u32 v8, v24, v10, s40
	v_add3_u32 v0, v25, v0, s40
	v_perm_b32 v8, v0, v8, s48
	v_perm_b32 v6, v11, v6, s48
	v_perm_b32 v9, v9, v14, s48
	v_perm_b32 v7, v7, v16, s48
	ds_write_b128 v214, v[2:5] offset:1024
	ds_write_b128 v214, v[6:9] offset:3072
	v_add_u32_e32 v0, 0, v204
	s_waitcnt vmcnt(3)
	ds_write_b128 v210, v[148:151] offset:49152
	s_waitcnt vmcnt(1)
	ds_write_b128 v210, v[156:159] offset:57344
	ds_write_b128 v0, v[144:147]
	ds_write_b128 v0, v[152:155] offset:12288
	v_add_u32_e32 v0, 0, v199
	v_mov_b32_e32 v14, v1
	v_mov_b32_e32 v15, v1
	s_waitcnt vmcnt(0)
	ds_write_b128 v0, v[160:163]
	v_mov_b32_e32 v0, v1
	v_mov_b32_e32 v2, v1
	v_mov_b32_e32 v3, v1
	v_mov_b32_e32 v4, v1
	v_mov_b32_e32 v5, v1
	v_mov_b32_e32 v6, v1
	v_mov_b32_e32 v7, v1
	v_mov_b32_e32 v8, v1
	v_mov_b32_e32 v9, v1
	v_mov_b32_e32 v10, v1
	v_mov_b32_e32 v11, v1
	v_mov_b32_e32 v12, v1
	v_mov_b32_e32 v13, v1
	v_mov_b64_e32 v[30:31], v[14:15]
	v_mov_b64_e32 v[46:47], v[14:15]
	v_mov_b64_e32 v[62:63], v[14:15]
	v_mov_b64_e32 v[78:79], v[14:15]
	v_mov_b64_e32 v[28:29], v[12:13]
	v_mov_b64_e32 v[26:27], v[10:11]
	v_mov_b64_e32 v[24:25], v[8:9]
	v_mov_b64_e32 v[22:23], v[6:7]
	v_mov_b64_e32 v[20:21], v[4:5]
	v_mov_b64_e32 v[18:19], v[2:3]
	v_mov_b64_e32 v[16:17], v[0:1]
	v_mov_b64_e32 v[44:45], v[12:13]
	v_mov_b64_e32 v[42:43], v[10:11]
	v_mov_b64_e32 v[40:41], v[8:9]
	v_mov_b64_e32 v[38:39], v[6:7]
	v_mov_b64_e32 v[36:37], v[4:5]
	v_mov_b64_e32 v[34:35], v[2:3]
	v_mov_b64_e32 v[32:33], v[0:1]
	v_mov_b64_e32 v[60:61], v[12:13]
	v_mov_b64_e32 v[58:59], v[10:11]
	v_mov_b64_e32 v[56:57], v[8:9]
	v_mov_b64_e32 v[54:55], v[6:7]
	v_mov_b64_e32 v[52:53], v[4:5]
	v_mov_b64_e32 v[50:51], v[2:3]
	v_mov_b64_e32 v[48:49], v[0:1]
	v_mov_b64_e32 v[76:77], v[12:13]
	v_mov_b64_e32 v[74:75], v[10:11]
	v_mov_b64_e32 v[72:73], v[8:9]
	v_mov_b64_e32 v[70:71], v[6:7]
	v_mov_b64_e32 v[68:69], v[4:5]
	v_mov_b64_e32 v[66:67], v[2:3]
	v_mov_b64_e32 v[64:65], v[0:1]
	s_waitcnt lgkmcnt(0)
	s_barrier
	s_cmp_lt_u32 s50, s44
	s_cselect_b64 s[14:15], -1, 0
	s_cmp_ge_u32 s50, s44
	s_cbranch_scc1 .LBB0_1127
	s_branch .LBB0_1126
